# c8
# speedup vs baseline: 1.0311x; 1.0013x over previous
.LBB1_3:
	s_and_b32 s8, s55, 6
	ds_read_b128 v[114:117], v77
	ds_read_b128 v[118:121], v77 offset:512
	ds_read_b128 v[122:125], v77 offset:1024
	ds_read_b128 v[126:129], v77 offset:1536
	ds_read_b64 v[90:91], v78
	ds_read_b64 v[92:93], v78 offset:8
	ds_read_b64 v[94:95], v78 offset:16
	ds_read_b64 v[96:97], v81
	ds_read_b64 v[98:99], v81 offset:8
	ds_read_b64 v[100:101], v81 offset:16
	v_lshl_add_u32 v89, s8, 9, v87
	ds_read_u16 v154, v89
	ds_read_b128 v[130:133], v77 offset:8192
	ds_read_b128 v[134:137], v77 offset:8704
	ds_read_b128 v[138:141], v77 offset:9216
	ds_read_b128 v[142:145], v77 offset:9728
	ds_read_b64 v[102:103], v80
	ds_read_b64 v[104:105], v80 offset:8
	ds_read_b64 v[106:107], v80 offset:16
	s_mov_b32 m0, s50
	ds_read_b64 v[108:109], v79
	ds_read_b64 v[110:111], v79 offset:8
	ds_read_b64 v[112:113], v79 offset:16
	v_lshl_add_u64 v[146:147], v[68:69], 0, s[14:15]
	ds_read_u16 v89, v89 offset:512
	global_load_lds_dwordx4 v[146:147], off
	v_lshl_add_u64 v[146:147], v[68:69], 0, s[16:17]
	s_mov_b32 m0, s51
	s_add_i32 s56, s37, s55
	global_load_lds_dwordx4 v[146:147], off
	v_lshl_add_u64 v[146:147], v[66:67], 0, s[12:13]
	v_lshl_add_u64 v[148:149], v[146:147], 0, s[18:19]
	s_mov_b32 m0, s52
	s_add_i32 s8, s56, 4
	global_load_lds_dwordx4 v[148:149], off
	v_lshl_add_u64 v[148:149], v[66:67], 0, s[10:11]
	v_lshl_add_u64 v[150:151], v[148:149], 0, s[18:19]
	s_mov_b32 m0, s53
	s_min_u32 s57, s8, 63
	global_load_lds_dwordx4 v[150:151], off
	v_lshl_add_u64 v[150:151], v[66:67], 0, s[4:5]
	v_lshl_add_u64 v[152:153], v[150:151], 0, s[18:19]
	s_mov_b32 m0, s54
	s_lshl_b32 s8, s57, 10
	global_load_lds_dwordx4 v[152:153], off
	v_lshl_add_u64 v[152:153], v[0:1], 0, s[8:9]
	s_lshl_b32 s8, s57, 9
	s_and_b32 s8, s8, 0xe00
	s_add_i32 m0, s49, s8
	s_add_i32 s57, s55, 4
	global_load_lds_dword v[152:153], off
	s_waitcnt vmcnt(6)
	s_waitcnt lgkmcnt(0)
	s_barrier
	s_setprio 1
	s_waitcnt lgkmcnt(0)
	v_mfma_scale_f32_32x32x64_f8f6f4 v[50:65], v[90:95], v[114:117], v[50:65], v154, v88 op_sel_hi:[0,0,0] cbsz:2 blgp:4
	v_mfma_scale_f32_32x32x64_f8f6f4 v[34:49], v[90:95], v[118:121], v[34:49], v154, v88 op_sel_hi:[0,0,0] cbsz:2 blgp:4
	v_mfma_scale_f32_32x32x64_f8f6f4 v[18:33], v[90:95], v[122:125], v[18:33], v154, v88 op_sel_hi:[0,0,0] cbsz:2 blgp:4
	v_mfma_scale_f32_32x32x64_f8f6f4 v[2:17], v[90:95], v[126:129], v[2:17], v154, v88 op_sel_hi:[0,0,0] cbsz:2 blgp:4
	v_mfma_scale_f32_32x32x64_f8f6f4 v[50:65], v[96:101], v[114:117], v[50:65], v154, v88 op_sel:[1,0,0] op_sel_hi:[0,0,0] cbsz:2 blgp:4
	v_mfma_scale_f32_32x32x64_f8f6f4 v[34:49], v[96:101], v[118:121], v[34:49], v154, v88 op_sel:[1,0,0] op_sel_hi:[0,0,0] cbsz:2 blgp:4
	v_mfma_scale_f32_32x32x64_f8f6f4 v[18:33], v[96:101], v[122:125], v[18:33], v154, v88 op_sel:[1,0,0] op_sel_hi:[0,0,0] cbsz:2 blgp:4
	v_mfma_scale_f32_32x32x64_f8f6f4 v[2:17], v[96:101], v[126:129], v[2:17], v154, v88 op_sel:[1,0,0] op_sel_hi:[0,0,0] cbsz:2 blgp:4
	v_mfma_scale_f32_32x32x64_f8f6f4 v[50:65], v[102:107], v[130:133], v[50:65], v89, v88 op_sel_hi:[0,0,0] cbsz:2 blgp:4
	v_mfma_scale_f32_32x32x64_f8f6f4 v[34:49], v[102:107], v[134:137], v[34:49], v89, v88 op_sel_hi:[0,0,0] cbsz:2 blgp:4
	v_mfma_scale_f32_32x32x64_f8f6f4 v[18:33], v[102:107], v[138:141], v[18:33], v89, v88 op_sel_hi:[0,0,0] cbsz:2 blgp:4
	v_mfma_scale_f32_32x32x64_f8f6f4 v[2:17], v[102:107], v[142:145], v[2:17], v89, v88 op_sel_hi:[0,0,0] cbsz:2 blgp:4
	v_mfma_scale_f32_32x32x64_f8f6f4 v[50:65], v[108:113], v[130:133], v[50:65], v89, v88 op_sel:[1,0,0] op_sel_hi:[0,0,0] cbsz:2 blgp:4
	v_mfma_scale_f32_32x32x64_f8f6f4 v[34:49], v[108:113], v[134:137], v[34:49], v89, v88 op_sel:[1,0,0] op_sel_hi:[0,0,0] cbsz:2 blgp:4
	v_mfma_scale_f32_32x32x64_f8f6f4 v[18:33], v[108:113], v[138:141], v[18:33], v89, v88 op_sel:[1,0,0] op_sel_hi:[0,0,0] cbsz:2 blgp:4
	v_mfma_scale_f32_32x32x64_f8f6f4 v[2:17], v[108:113], v[142:145], v[2:17], v89, v88 op_sel:[1,0,0] op_sel_hi:[0,0,0] cbsz:2 blgp:4
	s_setprio 0
	s_barrier
	s_add_i32 s8, s55, 2
	s_and_b32 s8, s8, 6
	ds_read_b128 v[114:117], v77 offset:40960
	ds_read_b128 v[118:121], v77 offset:41472
	ds_read_b128 v[122:125], v77 offset:41984
	ds_read_b128 v[126:129], v77 offset:42496
	ds_read_b64 v[90:91], v75
	ds_read_b64 v[92:93], v75 offset:8
	ds_read_b64 v[94:95], v75 offset:16
	ds_read_b64 v[96:97], v76
	ds_read_b64 v[98:99], v76 offset:8
	ds_read_b64 v[100:101], v76 offset:16
	v_lshl_add_u32 v89, s8, 9, v87
	ds_read_u16 v154, v89
	ds_read_b128 v[130:133], v77 offset:49152
	ds_read_b128 v[134:137], v77 offset:49664
	ds_read_b128 v[138:141], v77 offset:50176
	ds_read_b128 v[142:145], v77 offset:50688
	ds_read_b64 v[102:103], v74
	ds_read_b64 v[104:105], v74 offset:8
	ds_read_b64 v[106:107], v74 offset:16
	s_mov_b32 m0, s38
	ds_read_b64 v[108:109], v73
	ds_read_b64 v[110:111], v73 offset:8
	ds_read_b64 v[112:113], v73 offset:16
	v_lshl_add_u64 v[152:153], v[68:69], 0, s[20:21]
	ds_read_u16 v89, v89 offset:512
	global_load_lds_dwordx4 v[152:153], off
	v_lshl_add_u64 v[152:153], v[68:69], 0, s[22:23]
	s_mov_b32 m0, s39
	s_add_i32 s8, s56, 6
	global_load_lds_dwordx4 v[152:153], off
	v_lshl_add_u64 v[152:153], v[146:147], 0, s[24:25]
	s_mov_b32 m0, s40
	s_min_u32 s58, s8, 63
	global_load_lds_dwordx4 v[152:153], off
	v_lshl_add_u64 v[152:153], v[148:149], 0, s[24:25]
	s_mov_b32 m0, s41
	s_lshl_b32 s8, s58, 10
	global_load_lds_dwordx4 v[152:153], off
	v_lshl_add_u64 v[152:153], v[150:151], 0, s[24:25]
	s_mov_b32 m0, s42
	s_nop 0
	global_load_lds_dwordx4 v[152:153], off
	v_lshl_add_u64 v[152:153], v[0:1], 0, s[8:9]
	s_lshl_b32 s8, s58, 9
	s_and_b32 s8, s8, 0xe00
	s_add_i32 m0, s49, s8
	s_nop 0
	global_load_lds_dword v[152:153], off
	s_waitcnt vmcnt(6)
	s_waitcnt lgkmcnt(0)
	s_barrier
	s_setprio 1
	s_waitcnt lgkmcnt(0)
	v_mfma_scale_f32_32x32x64_f8f6f4 v[50:65], v[90:95], v[114:117], v[50:65], v154, v88 op_sel_hi:[0,0,0] cbsz:2 blgp:4
	v_mfma_scale_f32_32x32x64_f8f6f4 v[34:49], v[90:95], v[118:121], v[34:49], v154, v88 op_sel_hi:[0,0,0] cbsz:2 blgp:4
	v_mfma_scale_f32_32x32x64_f8f6f4 v[18:33], v[90:95], v[122:125], v[18:33], v154, v88 op_sel_hi:[0,0,0] cbsz:2 blgp:4
	v_mfma_scale_f32_32x32x64_f8f6f4 v[2:17], v[90:95], v[126:129], v[2:17], v154, v88 op_sel_hi:[0,0,0] cbsz:2 blgp:4
	v_mfma_scale_f32_32x32x64_f8f6f4 v[50:65], v[96:101], v[114:117], v[50:65], v154, v88 op_sel:[1,0,0] op_sel_hi:[0,0,0] cbsz:2 blgp:4
	v_mfma_scale_f32_32x32x64_f8f6f4 v[34:49], v[96:101], v[118:121], v[34:49], v154, v88 op_sel:[1,0,0] op_sel_hi:[0,0,0] cbsz:2 blgp:4
	v_mfma_scale_f32_32x32x64_f8f6f4 v[18:33], v[96:101], v[122:125], v[18:33], v154, v88 op_sel:[1,0,0] op_sel_hi:[0,0,0] cbsz:2 blgp:4
	v_mfma_scale_f32_32x32x64_f8f6f4 v[2:17], v[96:101], v[126:129], v[2:17], v154, v88 op_sel:[1,0,0] op_sel_hi:[0,0,0] cbsz:2 blgp:4
	v_mfma_scale_f32_32x32x64_f8f6f4 v[50:65], v[102:107], v[130:133], v[50:65], v89, v88 op_sel_hi:[0,0,0] cbsz:2 blgp:4
	v_mfma_scale_f32_32x32x64_f8f6f4 v[34:49], v[102:107], v[134:137], v[34:49], v89, v88 op_sel_hi:[0,0,0] cbsz:2 blgp:4
	v_mfma_scale_f32_32x32x64_f8f6f4 v[18:33], v[102:107], v[138:141], v[18:33], v89, v88 op_sel_hi:[0,0,0] cbsz:2 blgp:4
	v_mfma_scale_f32_32x32x64_f8f6f4 v[2:17], v[102:107], v[142:145], v[2:17], v89, v88 op_sel_hi:[0,0,0] cbsz:2 blgp:4
	v_mfma_scale_f32_32x32x64_f8f6f4 v[50:65], v[108:113], v[130:133], v[50:65], v89, v88 op_sel:[1,0,0] op_sel_hi:[0,0,0] cbsz:2 blgp:4
	v_mfma_scale_f32_32x32x64_f8f6f4 v[34:49], v[108:113], v[134:137], v[34:49], v89, v88 op_sel:[1,0,0] op_sel_hi:[0,0,0] cbsz:2 blgp:4
	v_mfma_scale_f32_32x32x64_f8f6f4 v[18:33], v[108:113], v[138:141], v[18:33], v89, v88 op_sel:[1,0,0] op_sel_hi:[0,0,0] cbsz:2 blgp:4
	v_mfma_scale_f32_32x32x64_f8f6f4 v[2:17], v[108:113], v[142:145], v[2:17], v89, v88 op_sel:[1,0,0] op_sel_hi:[0,0,0] cbsz:2 blgp:4
	s_setprio 0
	s_barrier
	s_and_b32 s8, s57, 6
	ds_read_b128 v[114:117], v86
	ds_read_b128 v[118:121], v86 offset:512
	ds_read_b128 v[122:125], v86 offset:1024
	ds_read_b128 v[126:129], v86 offset:1536
	ds_read_b64 v[90:91], v82
	ds_read_b64 v[92:93], v82 offset:8
	ds_read_b64 v[94:95], v82 offset:16
	ds_read_b64 v[96:97], v83
	ds_read_b64 v[98:99], v83 offset:8
	ds_read_b64 v[100:101], v83 offset:16
	v_lshl_add_u32 v89, s8, 9, v87
	ds_read_u16 v154, v89
	ds_read_b128 v[130:133], v86 offset:8192
	ds_read_b128 v[134:137], v86 offset:8704
	ds_read_b128 v[138:141], v86 offset:9216
	ds_read_b128 v[142:145], v86 offset:9728
	ds_read_b64 v[102:103], v84
	ds_read_b64 v[104:105], v84 offset:8
	ds_read_b64 v[106:107], v84 offset:16
	s_mov_b32 m0, s43
	ds_read_b64 v[108:109], v85
	ds_read_b64 v[110:111], v85 offset:8
	ds_read_b64 v[112:113], v85 offset:16
	v_lshl_add_u64 v[152:153], v[68:69], 0, s[26:27]
	ds_read_u16 v89, v89 offset:512
	global_load_lds_dwordx4 v[152:153], off
	s_mov_b32 m0, s44
	v_lshl_add_u64 v[146:147], v[146:147], 0, s[28:29]
	global_load_lds_dwordx4 v[68:69], off
	s_mov_b32 m0, s45
	s_add_i32 s56, s56, 8
	global_load_lds_dwordx4 v[146:147], off
	v_lshl_add_u64 v[146:147], v[148:149], 0, s[28:29]
	s_mov_b32 m0, s46
	s_min_u32 s56, s56, 63
	global_load_lds_dwordx4 v[146:147], off
	v_lshl_add_u64 v[146:147], v[150:151], 0, s[28:29]
	s_mov_b32 m0, s47
	s_lshl_b32 s8, s56, 10
	global_load_lds_dwordx4 v[146:147], off
	v_lshl_add_u64 v[146:147], v[0:1], 0, s[8:9]
	s_lshl_b32 s8, s56, 9
	s_and_b32 s8, s8, 0xe00
	s_add_i32 m0, s49, s8
	s_nop 0
	global_load_lds_dword v[146:147], off
	s_waitcnt vmcnt(6)
	s_waitcnt lgkmcnt(0)
	s_barrier
	s_setprio 1
	s_waitcnt lgkmcnt(0)
	v_mfma_scale_f32_32x32x64_f8f6f4 v[50:65], v[90:95], v[114:117], v[50:65], v154, v88 op_sel_hi:[0,0,0] cbsz:2 blgp:4
	v_mfma_scale_f32_32x32x64_f8f6f4 v[34:49], v[90:95], v[118:121], v[34:49], v154, v88 op_sel_hi:[0,0,0] cbsz:2 blgp:4
	v_mfma_scale_f32_32x32x64_f8f6f4 v[18:33], v[90:95], v[122:125], v[18:33], v154, v88 op_sel_hi:[0,0,0] cbsz:2 blgp:4
	v_mfma_scale_f32_32x32x64_f8f6f4 v[2:17], v[90:95], v[126:129], v[2:17], v154, v88 op_sel_hi:[0,0,0] cbsz:2 blgp:4
	v_mfma_scale_f32_32x32x64_f8f6f4 v[50:65], v[96:101], v[114:117], v[50:65], v154, v88 op_sel:[1,0,0] op_sel_hi:[0,0,0] cbsz:2 blgp:4
	v_mfma_scale_f32_32x32x64_f8f6f4 v[34:49], v[96:101], v[118:121], v[34:49], v154, v88 op_sel:[1,0,0] op_sel_hi:[0,0,0] cbsz:2 blgp:4
	v_mfma_scale_f32_32x32x64_f8f6f4 v[18:33], v[96:101], v[122:125], v[18:33], v154, v88 op_sel:[1,0,0] op_sel_hi:[0,0,0] cbsz:2 blgp:4
	v_mfma_scale_f32_32x32x64_f8f6f4 v[2:17], v[96:101], v[126:129], v[2:17], v154, v88 op_sel:[1,0,0] op_sel_hi:[0,0,0] cbsz:2 blgp:4
	v_mfma_scale_f32_32x32x64_f8f6f4 v[50:65], v[102:107], v[130:133], v[50:65], v89, v88 op_sel_hi:[0,0,0] cbsz:2 blgp:4
	v_mfma_scale_f32_32x32x64_f8f6f4 v[34:49], v[102:107], v[134:137], v[34:49], v89, v88 op_sel_hi:[0,0,0] cbsz:2 blgp:4
	v_mfma_scale_f32_32x32x64_f8f6f4 v[18:33], v[102:107], v[138:141], v[18:33], v89, v88 op_sel_hi:[0,0,0] cbsz:2 blgp:4
	v_mfma_scale_f32_32x32x64_f8f6f4 v[2:17], v[102:107], v[142:145], v[2:17], v89, v88 op_sel_hi:[0,0,0] cbsz:2 blgp:4
	v_mfma_scale_f32_32x32x64_f8f6f4 v[50:65], v[108:113], v[130:133], v[50:65], v89, v88 op_sel:[1,0,0] op_sel_hi:[0,0,0] cbsz:2 blgp:4
	v_mfma_scale_f32_32x32x64_f8f6f4 v[34:49], v[108:113], v[134:137], v[34:49], v89, v88 op_sel:[1,0,0] op_sel_hi:[0,0,0] cbsz:2 blgp:4
	v_mfma_scale_f32_32x32x64_f8f6f4 v[18:33], v[108:113], v[138:141], v[18:33], v89, v88 op_sel:[1,0,0] op_sel_hi:[0,0,0] cbsz:2 blgp:4
	v_mfma_scale_f32_32x32x64_f8f6f4 v[2:17], v[108:113], v[142:145], v[2:17], v89, v88 op_sel:[1,0,0] op_sel_hi:[0,0,0] cbsz:2 blgp:4
	s_setprio 0
	s_barrier
	s_add_i32 s48, s48, 3
	s_add_i32 s55, s55, 6
	v_lshl_add_u64 v[68:69], v[68:69], 0, s[6:7]
	s_cmp_lt_u32 s48, 27
	v_lshl_add_u64 v[66:67], v[66:67], 0, s[24:25]
	s_cbranch_scc1 .LBB1_3
	ds_read_b128 v[66:69], v77
	ds_read_b128 v[106:109], v77 offset:512
	ds_read_b128 v[110:113], v77 offset:1024
	ds_read_b128 v[114:117], v77 offset:1536
	ds_read_b64 v[82:83], v78
	ds_read_b64 v[84:85], v78 offset:8
	ds_read_b64 v[86:87], v78 offset:16
	ds_read_b64 v[88:89], v81
	ds_read_b64 v[90:91], v81 offset:8
	ds_read_b64 v[92:93], v81 offset:16
	v_add_u32_e32 v0, 0x1e800, v72
	ds_read_u16 v0, v0
	ds_read_b128 v[118:121], v77 offset:8192
	ds_read_b128 v[122:125], v77 offset:8704
	ds_read_b128 v[126:129], v77 offset:9216
	ds_read_b128 v[130:133], v77 offset:9728
	ds_read_b64 v[94:95], v80
	ds_read_b64 v[96:97], v80 offset:8
	ds_read_b64 v[98:99], v80 offset:16
	ds_read_b64 v[100:101], v79
	ds_read_b64 v[102:103], v79 offset:8
	ds_read_b64 v[104:105], v79 offset:16
	v_add_u32_e32 v1, 0x1ea00, v72
	ds_read_u16 v1, v1
	s_waitcnt vmcnt(0)
	s_waitcnt lgkmcnt(0)
	s_barrier
	s_setprio 1
	v_mov_b32_e32 v134, 0x7f7f7f7f
	s_waitcnt lgkmcnt(0)
	s_nop 0
	v_mfma_scale_f32_32x32x64_f8f6f4 v[50:65], v[82:87], v[66:69], v[50:65], v0, v134 op_sel_hi:[0,0,0] cbsz:2 blgp:4
	v_mfma_scale_f32_32x32x64_f8f6f4 v[34:49], v[82:87], v[106:109], v[34:49], v0, v134 op_sel_hi:[0,0,0] cbsz:2 blgp:4
	v_mfma_scale_f32_32x32x64_f8f6f4 v[18:33], v[82:87], v[110:113], v[18:33], v0, v134 op_sel_hi:[0,0,0] cbsz:2 blgp:4
	v_mfma_scale_f32_32x32x64_f8f6f4 v[2:17], v[82:87], v[114:117], v[2:17], v0, v134 op_sel_hi:[0,0,0] cbsz:2 blgp:4
	v_mfma_scale_f32_32x32x64_f8f6f4 v[50:65], v[88:93], v[66:69], v[50:65], v0, v134 op_sel:[1,0,0] op_sel_hi:[0,0,0] cbsz:2 blgp:4
	v_mfma_scale_f32_32x32x64_f8f6f4 v[34:49], v[88:93], v[106:109], v[34:49], v0, v134 op_sel:[1,0,0] op_sel_hi:[0,0,0] cbsz:2 blgp:4
	v_mfma_scale_f32_32x32x64_f8f6f4 v[18:33], v[88:93], v[110:113], v[18:33], v0, v134 op_sel:[1,0,0] op_sel_hi:[0,0,0] cbsz:2 blgp:4
	v_mfma_scale_f32_32x32x64_f8f6f4 v[2:17], v[88:93], v[114:117], v[2:17], v0, v134 op_sel:[1,0,0] op_sel_hi:[0,0,0] cbsz:2 blgp:4
	v_lshrrev_b32_e32 v0, 8, v1
	v_mfma_scale_f32_32x32x64_f8f6f4 v[50:65], v[94:99], v[118:121], v[50:65], v1, v134 op_sel_hi:[0,0,0] cbsz:2 blgp:4
	v_mfma_scale_f32_32x32x64_f8f6f4 v[34:49], v[94:99], v[122:125], v[34:49], v1, v134 op_sel_hi:[0,0,0] cbsz:2 blgp:4
	v_mfma_scale_f32_32x32x64_f8f6f4 v[18:33], v[94:99], v[126:129], v[18:33], v1, v134 op_sel_hi:[0,0,0] cbsz:2 blgp:4
	v_mfma_scale_f32_32x32x64_f8f6f4 v[2:17], v[94:99], v[130:133], v[2:17], v1, v134 op_sel_hi:[0,0,0] cbsz:2 blgp:4
	v_mfma_scale_f32_32x32x64_f8f6f4 v[50:65], v[100:105], v[118:121], v[50:65], v0, v134 op_sel_hi:[0,0,0] cbsz:2 blgp:4
	v_mfma_scale_f32_32x32x64_f8f6f4 v[34:49], v[100:105], v[122:125], v[34:49], v0, v134 op_sel_hi:[0,0,0] cbsz:2 blgp:4
	v_mfma_scale_f32_32x32x64_f8f6f4 v[18:33], v[100:105], v[126:129], v[18:33], v0, v134 op_sel_hi:[0,0,0] cbsz:2 blgp:4
	v_mfma_scale_f32_32x32x64_f8f6f4 v[2:17], v[100:105], v[130:133], v[2:17], v0, v134 op_sel_hi:[0,0,0] cbsz:2 blgp:4
	s_setprio 0
	s_barrier
	ds_read_b128 v[66:69], v77 offset:40960
	ds_read_b128 v[102:105], v77 offset:41472
	ds_read_b128 v[106:109], v77 offset:41984
	ds_read_b128 v[110:113], v77 offset:42496
	ds_read_b64 v[78:79], v75
	ds_read_b64 v[80:81], v75 offset:8
	ds_read_b64 v[82:83], v75 offset:16
	ds_read_b64 v[84:85], v76
	ds_read_b64 v[86:87], v76 offset:8
	ds_read_b64 v[88:89], v76 offset:16
	v_add_u32_e32 v0, 0x1ec00, v72
	ds_read_u16 v0, v0
	ds_read_b128 v[114:117], v77 offset:49152
	ds_read_b128 v[118:121], v77 offset:49664
	ds_read_b128 v[122:125], v77 offset:50176
	ds_read_b128 v[126:129], v77 offset:50688
	ds_read_b64 v[90:91], v74
	ds_read_b64 v[92:93], v74 offset:8
	ds_read_b64 v[94:95], v74 offset:16
	ds_read_b64 v[96:97], v73
	ds_read_b64 v[98:99], v73 offset:8
	ds_read_b64 v[100:101], v73 offset:16
	v_add_u32_e32 v1, 0x1ee00, v72
	ds_read_u16 v1, v1
	s_waitcnt vmcnt(0)
	s_waitcnt lgkmcnt(0)
	s_barrier
	s_setprio 1
	s_waitcnt lgkmcnt(0)
	v_mfma_scale_f32_32x32x64_f8f6f4 v[50:65], v[78:83], v[66:69], v[50:65], v0, v134 op_sel_hi:[0,0,0] cbsz:2 blgp:4
	v_mfma_scale_f32_32x32x64_f8f6f4 v[34:49], v[78:83], v[102:105], v[34:49], v0, v134 op_sel_hi:[0,0,0] cbsz:2 blgp:4
	v_mfma_scale_f32_32x32x64_f8f6f4 v[18:33], v[78:83], v[106:109], v[18:33], v0, v134 op_sel_hi:[0,0,0] cbsz:2 blgp:4
	v_mfma_scale_f32_32x32x64_f8f6f4 v[2:17], v[78:83], v[110:113], v[2:17], v0, v134 op_sel_hi:[0,0,0] cbsz:2 blgp:4
	v_mfma_scale_f32_32x32x64_f8f6f4 v[50:65], v[84:89], v[66:69], v[50:65], v0, v134 op_sel:[1,0,0] op_sel_hi:[0,0,0] cbsz:2 blgp:4
	v_mfma_scale_f32_32x32x64_f8f6f4 v[34:49], v[84:89], v[102:105], v[34:49], v0, v134 op_sel:[1,0,0] op_sel_hi:[0,0,0] cbsz:2 blgp:4
	v_mfma_scale_f32_32x32x64_f8f6f4 v[18:33], v[84:89], v[106:109], v[18:33], v0, v134 op_sel:[1,0,0] op_sel_hi:[0,0,0] cbsz:2 blgp:4
	v_mfma_scale_f32_32x32x64_f8f6f4 v[2:17], v[84:89], v[110:113], v[2:17], v0, v134 op_sel:[1,0,0] op_sel_hi:[0,0,0] cbsz:2 blgp:4
	v_lshrrev_b32_e32 v0, 8, v1
	v_mfma_scale_f32_32x32x64_f8f6f4 v[50:65], v[90:95], v[114:117], v[50:65], v1, v134 op_sel_hi:[0,0,0] cbsz:2 blgp:4
	v_mfma_scale_f32_32x32x64_f8f6f4 v[34:49], v[90:95], v[118:121], v[34:49], v1, v134 op_sel_hi:[0,0,0] cbsz:2 blgp:4
	v_mfma_scale_f32_32x32x64_f8f6f4 v[18:33], v[90:95], v[122:125], v[18:33], v1, v134 op_sel_hi:[0,0,0] cbsz:2 blgp:4
	v_mfma_scale_f32_32x32x64_f8f6f4 v[2:17], v[90:95], v[126:129], v[2:17], v1, v134 op_sel_hi:[0,0,0] cbsz:2 blgp:4
	v_mfma_scale_f32_32x32x64_f8f6f4 v[50:65], v[96:101], v[114:117], v[50:65], v0, v134 op_sel_hi:[0,0,0] cbsz:2 blgp:4
	v_mfma_scale_f32_32x32x64_f8f6f4 v[34:49], v[96:101], v[118:121], v[34:49], v0, v134 op_sel_hi:[0,0,0] cbsz:2 blgp:4
	v_mfma_scale_f32_32x32x64_f8f6f4 v[18:33], v[96:101], v[122:125], v[18:33], v0, v134 op_sel_hi:[0,0,0] cbsz:2 blgp:4
	v_mfma_scale_f32_32x32x64_f8f6f4 v[2:17], v[96:101], v[126:129], v[2:17], v0, v134 op_sel_hi:[0,0,0] cbsz:2 blgp:4
	s_setprio 0
	s_barrier
	s_cmpk_gt_u32 s33, 0xff
	s_cbranch_scc1 .LBB1_6
	s_barrier
